# speedup vs baseline: 1.0617x; 1.0272x over previous
_Z6k_prep5PrepP:
	s_load_dwordx16 s[36:51], s[0:1], 0x0
	s_load_dwordx16 s[8:23], s[0:1], 0x40
	s_cmp_gt_i32 s3, 3
	s_mov_b64 s[4:5], -1
	s_cbranch_scc0 .LBB0_220
	s_cmp_lt_i32 s3, 5
	s_cbranch_scc1 .LBB0_208
	s_cmp_lg_u32 s3, 5
	s_cbranch_scc0 .LBB0_196
	s_cmp_gt_u32 s3, 9
	s_cbranch_scc0 .LBB0_184
	s_cmp_lt_i32 s3, 11
	s_cbranch_scc1 .LBB0_172
	s_cmp_lg_u32 s3, 11
	s_cbranch_scc0 .LBB0_160
	s_cmp_gt_u32 s3, 14
	s_cbranch_scc0 .LBB0_148
	s_cmp_gt_u32 s3, 16
	s_cbranch_scc0 .LBB0_136
	s_cmp_lt_i32 s3, 19
	s_cbranch_scc1 .LBB0_111
	s_cmp_lt_i32 s3, 20
	s_cbranch_scc1 .LBB0_99
	s_cmp_lg_u32 s3, 20
	s_cbranch_scc0 .LBB0_87
	s_cmp_gt_u32 s3, 29
	s_cbranch_scc0 .LBB0_75
	s_load_dwordx16 s[52:67], s[0:1], 0x80
	s_load_dwordx16 s[68:83], s[0:1], 0xc0
	s_load_dwordx4 s[24:27], s[0:1], 0x100
	s_cmp_lt_i32 s3, 33
	s_mov_b64 s[0:1], -1
	s_cbranch_scc1 .LBB0_42
	s_cmp_lt_i32 s3, 34
	s_cbranch_scc1 .LBB0_33
	s_mov_b32 s28, s3
	s_cmp_lt_i32 s3, 35
	s_cbranch_scc1 .LBB0_27
	s_cmp_eq_u32 s28, 35
	s_cbranch_scc0 .LBB0_26
	s_cmp_lg_u32 s2, 0
	s_cbranch_scc1 .LBB0_26
	s_movk_i32 s0, 0xc0
	v_cmp_gt_u32_e32 vcc, s0, v0
	v_and_b32_e32 v1, 63, v0
	s_and_saveexec_b64 s[0:1], vcc
	s_cbranch_execz .LBB0_21
	v_lshlrev_b32_e32 v2, 8, v0
	v_lshlrev_b32_e32 v6, 2, v1
	s_mov_b32 s3, 0x3c000
	v_mov_b32_e32 v3, 0
	v_and_or_b32 v2, v2, s3, v6
	v_lshlrev_b32_e32 v7, 2, v0
	s_waitcnt lgkmcnt(0)
	global_load_dword v132, v6, s[72:73]
	global_load_dword v133, v6, s[74:75]
	global_load_dword v134, v7, s[76:77]
	v_lshl_add_u64 v[4:5], s[36:37], 0, v[2:3]
	s_mov_b64 s[4:5], 0x1000
	v_lshl_add_u64 v[4:5], v[4:5], 0, s[4:5]
	s_mov_b64 s[4:5], 0x2000
	v_lshl_add_u64 v[8:9], v[4:5], 0, s[4:5]
	global_load_dword v68, v[4:5], off offset:-4096
	global_load_dword v69, v[4:5], off offset:-3840
	global_load_dword v70, v[4:5], off offset:-3584
	global_load_dword v71, v[4:5], off offset:-3328
	global_load_dword v72, v[4:5], off offset:-3072
	global_load_dword v73, v[4:5], off offset:-2816
	global_load_dword v74, v[4:5], off offset:-2560
	global_load_dword v75, v[4:5], off offset:-2304
	global_load_dword v76, v[4:5], off offset:-2048
	global_load_dword v77, v[4:5], off offset:-1792
	global_load_dword v78, v[4:5], off offset:-1536
	global_load_dword v79, v[4:5], off offset:-1280
	global_load_dword v80, v[4:5], off offset:-1024
	global_load_dword v81, v[4:5], off offset:-768
	global_load_dword v82, v[4:5], off offset:-512
	global_load_dword v83, v[4:5], off offset:-256
	global_load_dword v84, v[4:5], off
	global_load_dword v85, v[4:5], off offset:256
	global_load_dword v86, v[4:5], off offset:512
	global_load_dword v87, v[4:5], off offset:768
	global_load_dword v88, v[4:5], off offset:1024
	global_load_dword v89, v[4:5], off offset:1280
	global_load_dword v90, v[4:5], off offset:1536
	global_load_dword v91, v[4:5], off offset:1792
	global_load_dword v92, v[4:5], off offset:2048
	global_load_dword v93, v[4:5], off offset:2304
	global_load_dword v94, v[4:5], off offset:2560
	global_load_dword v95, v[4:5], off offset:2816
	global_load_dword v96, v[4:5], off offset:3072
	global_load_dword v97, v[4:5], off offset:3328
	global_load_dword v98, v[4:5], off offset:3584
	global_load_dword v99, v[4:5], off offset:3840
	global_load_dword v100, v[8:9], off offset:-4096
	global_load_dword v101, v[8:9], off offset:-3840
	global_load_dword v102, v[8:9], off offset:-3584
	global_load_dword v103, v[8:9], off offset:-3328
	global_load_dword v104, v[8:9], off offset:-3072
	global_load_dword v105, v[8:9], off offset:-2816
	global_load_dword v106, v[8:9], off offset:-2560
	global_load_dword v107, v[8:9], off offset:-2304
	global_load_dword v108, v[8:9], off offset:-2048
	global_load_dword v109, v[8:9], off offset:-1792
	global_load_dword v110, v[8:9], off offset:-1536
	global_load_dword v111, v[8:9], off offset:-1280
	global_load_dword v112, v[8:9], off offset:-1024
	global_load_dword v113, v[8:9], off offset:-768
	global_load_dword v114, v[8:9], off offset:-512
	global_load_dword v115, v[8:9], off offset:-256
	global_load_dword v116, v[8:9], off
	global_load_dword v117, v[8:9], off offset:256
	global_load_dword v118, v[8:9], off offset:512
	global_load_dword v119, v[8:9], off offset:768
	global_load_dword v120, v[8:9], off offset:1024
	global_load_dword v121, v[8:9], off offset:1280
	global_load_dword v122, v[8:9], off offset:1536
	global_load_dword v123, v[8:9], off offset:1792
	global_load_dword v124, v[8:9], off offset:2048
	global_load_dword v125, v[8:9], off offset:2304
	global_load_dword v126, v[8:9], off offset:2560
	global_load_dword v127, v[8:9], off offset:2816
	global_load_dword v128, v[8:9], off offset:3072
	global_load_dword v129, v[8:9], off offset:3328
	global_load_dword v130, v[8:9], off offset:3584
	global_load_dword v131, v[8:9], off offset:3840
	v_mov_b32_e32 v2, 0
	s_waitcnt vmcnt(56)
	v_readlane_b32 s84, v132, 0
	v_readlane_b32 s85, v133, 0
	v_readlane_b32 s86, v132, 1
	v_readlane_b32 s87, v133, 1
	v_readlane_b32 s88, v132, 2
	v_readlane_b32 s89, v133, 2
	v_readlane_b32 s90, v132, 3
	v_readlane_b32 s91, v133, 3
	v_readlane_b32 s92, v132, 4
	v_readlane_b32 s93, v133, 4
	v_readlane_b32 s94, v132, 5
	v_readlane_b32 s95, v133, 5
	v_readlane_b32 s96, v132, 6
	v_readlane_b32 s97, v133, 6
	v_readlane_b32 s98, v132, 7
	v_readlane_b32 s99, v133, 7
	v_pk_fma_f32 v[2:3], v[68:69], s[84:85], v[2:3] op_sel_hi:[0,1,1]
	v_pk_fma_f32 v[2:3], v[68:69], s[86:87], v[2:3] op_sel:[1,0,0]
	v_pk_fma_f32 v[2:3], v[70:71], s[88:89], v[2:3] op_sel_hi:[0,1,1]
	v_pk_fma_f32 v[2:3], v[70:71], s[90:91], v[2:3] op_sel:[1,0,0]
	v_pk_fma_f32 v[2:3], v[72:73], s[92:93], v[2:3] op_sel_hi:[0,1,1]
	v_pk_fma_f32 v[2:3], v[72:73], s[94:95], v[2:3] op_sel:[1,0,0]
	v_pk_fma_f32 v[2:3], v[74:75], s[96:97], v[2:3] op_sel_hi:[0,1,1]
	v_pk_fma_f32 v[2:3], v[74:75], s[98:99], v[2:3] op_sel:[1,0,0]
	s_waitcnt vmcnt(48)
	v_readlane_b32 s84, v132, 8
	v_readlane_b32 s85, v133, 8
	v_readlane_b32 s86, v132, 9
	v_readlane_b32 s87, v133, 9
	v_readlane_b32 s88, v132, 10
	v_readlane_b32 s89, v133, 10
	v_readlane_b32 s90, v132, 11
	v_readlane_b32 s91, v133, 11
	v_readlane_b32 s92, v132, 12
	v_readlane_b32 s93, v133, 12
	v_readlane_b32 s94, v132, 13
	v_readlane_b32 s95, v133, 13
	v_readlane_b32 s96, v132, 14
	v_readlane_b32 s97, v133, 14
	v_readlane_b32 s98, v132, 15
	v_readlane_b32 s99, v133, 15
	v_pk_fma_f32 v[2:3], v[76:77], s[84:85], v[2:3] op_sel_hi:[0,1,1]
	v_pk_fma_f32 v[2:3], v[76:77], s[86:87], v[2:3] op_sel:[1,0,0]
	v_pk_fma_f32 v[2:3], v[78:79], s[88:89], v[2:3] op_sel_hi:[0,1,1]
	v_pk_fma_f32 v[2:3], v[78:79], s[90:91], v[2:3] op_sel:[1,0,0]
	v_pk_fma_f32 v[2:3], v[80:81], s[92:93], v[2:3] op_sel_hi:[0,1,1]
	v_pk_fma_f32 v[2:3], v[80:81], s[94:95], v[2:3] op_sel:[1,0,0]
	v_pk_fma_f32 v[2:3], v[82:83], s[96:97], v[2:3] op_sel_hi:[0,1,1]
	v_pk_fma_f32 v[2:3], v[82:83], s[98:99], v[2:3] op_sel:[1,0,0]
	s_waitcnt vmcnt(40)
	v_readlane_b32 s84, v132, 16
	v_readlane_b32 s85, v133, 16
	v_readlane_b32 s86, v132, 17
	v_readlane_b32 s87, v133, 17
	v_readlane_b32 s88, v132, 18
	v_readlane_b32 s89, v133, 18
	v_readlane_b32 s90, v132, 19
	v_readlane_b32 s91, v133, 19
	v_readlane_b32 s92, v132, 20
	v_readlane_b32 s93, v133, 20
	v_readlane_b32 s94, v132, 21
	v_readlane_b32 s95, v133, 21
	v_readlane_b32 s96, v132, 22
	v_readlane_b32 s97, v133, 22
	v_readlane_b32 s98, v132, 23
	v_readlane_b32 s99, v133, 23
	v_pk_fma_f32 v[2:3], v[84:85], s[84:85], v[2:3] op_sel_hi:[0,1,1]
	v_pk_fma_f32 v[2:3], v[84:85], s[86:87], v[2:3] op_sel:[1,0,0]
	v_pk_fma_f32 v[2:3], v[86:87], s[88:89], v[2:3] op_sel_hi:[0,1,1]
	v_pk_fma_f32 v[2:3], v[86:87], s[90:91], v[2:3] op_sel:[1,0,0]
	v_pk_fma_f32 v[2:3], v[88:89], s[92:93], v[2:3] op_sel_hi:[0,1,1]
	v_pk_fma_f32 v[2:3], v[88:89], s[94:95], v[2:3] op_sel:[1,0,0]
	v_pk_fma_f32 v[2:3], v[90:91], s[96:97], v[2:3] op_sel_hi:[0,1,1]
	v_pk_fma_f32 v[2:3], v[90:91], s[98:99], v[2:3] op_sel:[1,0,0]
	s_waitcnt vmcnt(32)
	v_readlane_b32 s84, v132, 24
	v_readlane_b32 s85, v133, 24
	v_readlane_b32 s86, v132, 25
	v_readlane_b32 s87, v133, 25
	v_readlane_b32 s88, v132, 26
	v_readlane_b32 s89, v133, 26
	v_readlane_b32 s90, v132, 27
	v_readlane_b32 s91, v133, 27
	v_readlane_b32 s92, v132, 28
	v_readlane_b32 s93, v133, 28
	v_readlane_b32 s94, v132, 29
	v_readlane_b32 s95, v133, 29
	v_readlane_b32 s96, v132, 30
	v_readlane_b32 s97, v133, 30
	v_readlane_b32 s98, v132, 31
	v_readlane_b32 s99, v133, 31
	v_pk_fma_f32 v[2:3], v[92:93], s[84:85], v[2:3] op_sel_hi:[0,1,1]
	v_pk_fma_f32 v[2:3], v[92:93], s[86:87], v[2:3] op_sel:[1,0,0]
	v_pk_fma_f32 v[2:3], v[94:95], s[88:89], v[2:3] op_sel_hi:[0,1,1]
	v_pk_fma_f32 v[2:3], v[94:95], s[90:91], v[2:3] op_sel:[1,0,0]
	v_pk_fma_f32 v[2:3], v[96:97], s[92:93], v[2:3] op_sel_hi:[0,1,1]
	v_pk_fma_f32 v[2:3], v[96:97], s[94:95], v[2:3] op_sel:[1,0,0]
	v_pk_fma_f32 v[2:3], v[98:99], s[96:97], v[2:3] op_sel_hi:[0,1,1]
	v_pk_fma_f32 v[2:3], v[98:99], s[98:99], v[2:3] op_sel:[1,0,0]
	s_waitcnt vmcnt(24)
	v_readlane_b32 s84, v132, 32
	v_readlane_b32 s85, v133, 32
	v_readlane_b32 s86, v132, 33
	v_readlane_b32 s87, v133, 33
	v_readlane_b32 s88, v132, 34
	v_readlane_b32 s89, v133, 34
	v_readlane_b32 s90, v132, 35
	v_readlane_b32 s91, v133, 35
	v_readlane_b32 s92, v132, 36
	v_readlane_b32 s93, v133, 36
	v_readlane_b32 s94, v132, 37
	v_readlane_b32 s95, v133, 37
	v_readlane_b32 s96, v132, 38
	v_readlane_b32 s97, v133, 38
	v_readlane_b32 s98, v132, 39
	v_readlane_b32 s99, v133, 39
	v_pk_fma_f32 v[2:3], v[100:101], s[84:85], v[2:3] op_sel_hi:[0,1,1]
	v_pk_fma_f32 v[2:3], v[100:101], s[86:87], v[2:3] op_sel:[1,0,0]
	v_pk_fma_f32 v[2:3], v[102:103], s[88:89], v[2:3] op_sel_hi:[0,1,1]
	v_pk_fma_f32 v[2:3], v[102:103], s[90:91], v[2:3] op_sel:[1,0,0]
	v_pk_fma_f32 v[2:3], v[104:105], s[92:93], v[2:3] op_sel_hi:[0,1,1]
	v_pk_fma_f32 v[2:3], v[104:105], s[94:95], v[2:3] op_sel:[1,0,0]
	v_pk_fma_f32 v[2:3], v[106:107], s[96:97], v[2:3] op_sel_hi:[0,1,1]
	v_pk_fma_f32 v[2:3], v[106:107], s[98:99], v[2:3] op_sel:[1,0,0]
	s_waitcnt vmcnt(16)
	v_readlane_b32 s84, v132, 40
	v_readlane_b32 s85, v133, 40
	v_readlane_b32 s86, v132, 41
	v_readlane_b32 s87, v133, 41
	v_readlane_b32 s88, v132, 42
	v_readlane_b32 s89, v133, 42
	v_readlane_b32 s90, v132, 43
	v_readlane_b32 s91, v133, 43
	v_readlane_b32 s92, v132, 44
	v_readlane_b32 s93, v133, 44
	v_readlane_b32 s94, v132, 45
	v_readlane_b32 s95, v133, 45
	v_readlane_b32 s96, v132, 46
	v_readlane_b32 s97, v133, 46
	v_readlane_b32 s98, v132, 47
	v_readlane_b32 s99, v133, 47
	v_pk_fma_f32 v[2:3], v[108:109], s[84:85], v[2:3] op_sel_hi:[0,1,1]
	v_pk_fma_f32 v[2:3], v[108:109], s[86:87], v[2:3] op_sel:[1,0,0]
	v_pk_fma_f32 v[2:3], v[110:111], s[88:89], v[2:3] op_sel_hi:[0,1,1]
	v_pk_fma_f32 v[2:3], v[110:111], s[90:91], v[2:3] op_sel:[1,0,0]
	v_pk_fma_f32 v[2:3], v[112:113], s[92:93], v[2:3] op_sel_hi:[0,1,1]
	v_pk_fma_f32 v[2:3], v[112:113], s[94:95], v[2:3] op_sel:[1,0,0]
	v_pk_fma_f32 v[2:3], v[114:115], s[96:97], v[2:3] op_sel_hi:[0,1,1]
	v_pk_fma_f32 v[2:3], v[114:115], s[98:99], v[2:3] op_sel:[1,0,0]
	s_waitcnt vmcnt(8)
	v_readlane_b32 s84, v132, 48
	v_readlane_b32 s85, v133, 48
	v_readlane_b32 s86, v132, 49
	v_readlane_b32 s87, v133, 49
	v_readlane_b32 s88, v132, 50
	v_readlane_b32 s89, v133, 50
	v_readlane_b32 s90, v132, 51
	v_readlane_b32 s91, v133, 51
	v_readlane_b32 s92, v132, 52
	v_readlane_b32 s93, v133, 52
	v_readlane_b32 s94, v132, 53
	v_readlane_b32 s95, v133, 53
	v_readlane_b32 s96, v132, 54
	v_readlane_b32 s97, v133, 54
	v_readlane_b32 s98, v132, 55
	v_readlane_b32 s99, v133, 55
	v_pk_fma_f32 v[2:3], v[116:117], s[84:85], v[2:3] op_sel_hi:[0,1,1]
	v_pk_fma_f32 v[2:3], v[116:117], s[86:87], v[2:3] op_sel:[1,0,0]
	v_pk_fma_f32 v[2:3], v[118:119], s[88:89], v[2:3] op_sel_hi:[0,1,1]
	v_pk_fma_f32 v[2:3], v[118:119], s[90:91], v[2:3] op_sel:[1,0,0]
	v_pk_fma_f32 v[2:3], v[120:121], s[92:93], v[2:3] op_sel_hi:[0,1,1]
	v_pk_fma_f32 v[2:3], v[120:121], s[94:95], v[2:3] op_sel:[1,0,0]
	v_pk_fma_f32 v[2:3], v[122:123], s[96:97], v[2:3] op_sel_hi:[0,1,1]
	v_pk_fma_f32 v[2:3], v[122:123], s[98:99], v[2:3] op_sel:[1,0,0]
	s_waitcnt vmcnt(0)
	v_readlane_b32 s84, v132, 56
	v_readlane_b32 s85, v133, 56
	v_readlane_b32 s86, v132, 57
	v_readlane_b32 s87, v133, 57
	v_readlane_b32 s88, v132, 58
	v_readlane_b32 s89, v133, 58
	v_readlane_b32 s90, v132, 59
	v_readlane_b32 s91, v133, 59
	v_readlane_b32 s92, v132, 60
	v_readlane_b32 s93, v133, 60
	v_readlane_b32 s94, v132, 61
	v_readlane_b32 s95, v133, 61
	v_readlane_b32 s96, v132, 62
	v_readlane_b32 s97, v133, 62
	v_readlane_b32 s98, v132, 63
	v_readlane_b32 s99, v133, 63
	v_pk_fma_f32 v[2:3], v[124:125], s[84:85], v[2:3] op_sel_hi:[0,1,1]
	v_pk_fma_f32 v[2:3], v[124:125], s[86:87], v[2:3] op_sel:[1,0,0]
	v_pk_fma_f32 v[2:3], v[126:127], s[88:89], v[2:3] op_sel_hi:[0,1,1]
	v_pk_fma_f32 v[2:3], v[126:127], s[90:91], v[2:3] op_sel:[1,0,0]
	v_pk_fma_f32 v[2:3], v[128:129], s[92:93], v[2:3] op_sel_hi:[0,1,1]
	v_pk_fma_f32 v[2:3], v[128:129], s[94:95], v[2:3] op_sel:[1,0,0]
	v_pk_fma_f32 v[2:3], v[130:131], s[96:97], v[2:3] op_sel_hi:[0,1,1]
	v_pk_fma_f32 v[2:3], v[130:131], s[98:99], v[2:3] op_sel:[1,0,0]
	v_add_f32_e32 v3, v3, v134
	v_lshlrev_b32_e32 v5, 2, v0
	s_movk_i32 s3, 0xf00
	v_and_or_b32 v5, v5, s3, v6
	v_add_u32_e32 v4, 64, v5
	ds_write2st64_b32 v4, v3, v2 offset0:102 offset1:105

.Lmy_j34:
	v_bfe_u32 v12, v2, 3, 5
	v_ashrrev_i32_e32 v13, 5, v2
	v_lshrrev_b32_e32 v14, 5, v2
	v_and_b32_e32 v13, -16, v13
	v_and_b32_e32 v14, 8, v14
	v_mul_u32_u24_e32 v15, 0x180, v12
	v_mad_u32_u24 v16, v12, s3, v3
	v_cmp_gt_u32_e32 vcc, 16, v12
	v_or3_b32 v14, v14, v1, v13
	s_nop 0
	v_cndmask_b32_e32 v15, v16, v15, vcc
	v_add_u32_e32 v14, v14, v15
	v_cndmask_b32_e32 v13, v8, v9, vcc
	v_cndmask_b32_e32 v12, v10, v11, vcc
	v_ashrrev_i32_e32 v15, 31, v14
	v_lshl_add_u64 v[12:13], v[14:15], 2, v[12:13]
	global_load_dword v100, v[12:13], off
	v_add_u32_e32 v2, 0x1000, v2
	v_bfe_u32 v12, v2, 3, 5
	v_ashrrev_i32_e32 v13, 5, v2
	v_lshrrev_b32_e32 v14, 5, v2
	v_and_b32_e32 v13, -16, v13
	v_and_b32_e32 v14, 8, v14
	v_mul_u32_u24_e32 v15, 0x180, v12
	v_mad_u32_u24 v16, v12, s3, v3
	v_cmp_gt_u32_e32 vcc, 16, v12
	v_or3_b32 v14, v14, v1, v13
	s_nop 0
	v_cndmask_b32_e32 v15, v16, v15, vcc
	v_add_u32_e32 v14, v14, v15
	v_cndmask_b32_e32 v13, v8, v9, vcc
	v_cndmask_b32_e32 v12, v10, v11, vcc
	v_ashrrev_i32_e32 v15, 31, v14
	v_lshl_add_u64 v[12:13], v[14:15], 2, v[12:13]
	global_load_dword v101, v[12:13], off
	v_add_u32_e32 v2, 0x1000, v2
	v_bfe_u32 v12, v2, 3, 5
	v_ashrrev_i32_e32 v13, 5, v2
	v_lshrrev_b32_e32 v14, 5, v2
	v_and_b32_e32 v13, -16, v13
	v_and_b32_e32 v14, 8, v14
	v_mul_u32_u24_e32 v15, 0x180, v12
	v_mad_u32_u24 v16, v12, s3, v3
	v_cmp_gt_u32_e32 vcc, 16, v12
	v_or3_b32 v14, v14, v1, v13
	s_nop 0
	v_cndmask_b32_e32 v15, v16, v15, vcc
	v_add_u32_e32 v14, v14, v15
	v_cndmask_b32_e32 v13, v8, v9, vcc
	v_cndmask_b32_e32 v12, v10, v11, vcc
	v_ashrrev_i32_e32 v15, 31, v14
	v_lshl_add_u64 v[12:13], v[14:15], 2, v[12:13]
	global_load_dword v102, v[12:13], off
	s_waitcnt vmcnt(2)
	v_cvt_f16_f32_e32 v13, v100
	v_cvt_f32_f16_e32 v15, v13
	global_store_short v[4:5], v13, off
	v_lshl_add_u64 v[4:5], v[4:5], 0, s[6:7]
	v_sub_f32_e32 v12, v100, v15
	v_cvt_f16_f32_e32 v12, v12
	global_store_short v[6:7], v12, off
	v_lshl_add_u64 v[6:7], v[6:7], 0, s[6:7]
	s_waitcnt vmcnt(1)
	v_cvt_f16_f32_e32 v13, v101
	v_cvt_f32_f16_e32 v15, v13
	global_store_short v[4:5], v13, off
	v_lshl_add_u64 v[4:5], v[4:5], 0, s[6:7]
	v_sub_f32_e32 v12, v101, v15
	v_cvt_f16_f32_e32 v12, v12
	global_store_short v[6:7], v12, off
	v_lshl_add_u64 v[6:7], v[6:7], 0, s[6:7]
	s_waitcnt vmcnt(0)
	v_cvt_f16_f32_e32 v13, v102
	v_cvt_f32_f16_e32 v15, v13
	global_store_short v[4:5], v13, off
	v_lshl_add_u64 v[4:5], v[4:5], 0, s[6:7]
	v_sub_f32_e32 v12, v102, v15
	v_cvt_f16_f32_e32 v12, v12
	global_store_short v[6:7], v12, off
	v_lshl_add_u64 v[6:7], v[6:7], 0, s[6:7]

.Lmy_j33a:
	v_ashrrev_i32_e32 v9, 5, v8
	v_add_u32_e32 v10, v1, v9
	v_ashrrev_i32_e32 v11, 31, v10
	v_lshl_add_u64 v[10:11], v[10:11], 2, v[4:5]
	global_load_dword v100, v[10:11], off
	v_add_u32_e32 v8, 0x1000, v8
	v_ashrrev_i32_e32 v9, 5, v8
	v_add_u32_e32 v10, v1, v9
	v_ashrrev_i32_e32 v11, 31, v10
	v_lshl_add_u64 v[10:11], v[10:11], 2, v[4:5]
	global_load_dword v101, v[10:11], off
	v_add_u32_e32 v8, 0x1000, v8
	v_ashrrev_i32_e32 v9, 5, v8
	v_add_u32_e32 v10, v1, v9
	v_ashrrev_i32_e32 v11, 31, v10
	v_lshl_add_u64 v[10:11], v[10:11], 2, v[4:5]
	global_load_dword v102, v[10:11], off
	s_waitcnt vmcnt(2)
	global_store_dword v[6:7], v100, off
	v_lshl_add_u64 v[6:7], v[6:7], 0, s[6:7]
	s_waitcnt vmcnt(1)
	global_store_dword v[6:7], v101, off
	v_lshl_add_u64 v[6:7], v[6:7], 0, s[6:7]
	s_waitcnt vmcnt(0)
	global_store_dword v[6:7], v102, off
	v_lshl_add_u64 v[6:7], v[6:7], 0, s[6:7]

.Lmy_j33b:
	global_load_dword v100, v[4:5], off
	v_add_u32_e32 v1, 0x1000, v1
	v_cmp_ge_i32_e32 vcc, s26, v1
	v_lshl_add_u64 v[4:5], v[4:5], 0, s[6:7]
	s_and_saveexec_b64 s[4:5], vcc
	global_load_dword v101, v[4:5], off
	s_or_b64 exec, exec, s[4:5]
	s_waitcnt vmcnt(0)
	global_store_dword v[2:3], v100, off
	v_lshl_add_u64 v[2:3], v[2:3], 0, s[6:7]
	s_and_saveexec_b64 s[4:5], vcc
	global_store_dword v[2:3], v101, off
	s_or_b64 exec, exec, s[4:5]

.LBB0_42:
	s_andn2_b64 vcc, exec, s[0:1]
	s_cbranch_vccnz .LBB0_74
	s_cmp_lt_i32 s3, 31
	s_mov_b64 s[0:1], -1
	s_cbranch_scc1 .LBB0_70
	s_mov_b32 s28, s3
	s_cmp_gt_i32 s3, 31
	s_cbranch_scc0 .LBB0_65
	s_waitcnt lgkmcnt(0)
	v_lshlrev_b32_e32 v2, 4, v0
	v_mov_b32_e32 v3, 0
	v_lshl_add_u64 v[2:3], s[58:59], 0, v[2:3]
	s_mov_b64 s[4:5], 0x1000
	v_lshl_add_u64 v[4:5], v[2:3], 0, s[4:5]
	s_mov_b64 s[4:5], 0x3000
	v_lshl_add_u64 v[6:7], v[2:3], 0, s[4:5]
	s_mov_b64 s[4:5], 0x5000
	v_lshl_add_u64 v[8:9], v[2:3], 0, s[4:5]
	global_load_dwordx4 v[68:71], v[4:5], off offset:-4096
	global_load_dwordx4 v[72:75], v[4:5], off
	global_load_dwordx4 v[76:79], v[6:7], off offset:-4096
	global_load_dwordx4 v[80:83], v[6:7], off
	global_load_dwordx4 v[84:87], v[8:9], off offset:-4096
	global_load_dwordx4 v[88:91], v[8:9], off
	s_mul_i32 s29, s2, 0x180
	v_add_u32_e32 v10, s29, v0
	v_ashrrev_i32_e32 v11, 31, v10
	v_lshl_add_u64 v[10:11], v[10:11], 2, s[56:57]
	global_load_dword v98, v[10:11], off
	s_movk_i32 s0, 0x80
	v_cmp_gt_u32_e32 vcc, s0, v0
	s_and_saveexec_b64 s[6:7], vcc
	global_load_dword v99, v[10:11], off offset:1024
	s_or_b64 exec, exec, s[6:7]
	s_movk_i32 s3, 0x604
	v_mov_b32_e32 v12, v0
	v_mul_u32_u24_e32 v13, 0xaaab, v12
	v_lshrrev_b32_e32 v13, 22, v13
	v_mul_u32_u24_e32 v14, 0x60, v13
	v_sub_u32_e32 v14, v12, v14
	v_lshlrev_b32_e32 v14, 4, v14
	v_mad_u32_u24 v92, v13, s3, v14
	v_add_u32_e32 v12, 256, v0
	v_mul_u32_u24_e32 v13, 0xaaab, v12
	v_lshrrev_b32_e32 v13, 22, v13
	v_mul_u32_u24_e32 v14, 0x60, v13
	v_sub_u32_e32 v14, v12, v14
	v_lshlrev_b32_e32 v14, 4, v14
	v_mad_u32_u24 v93, v13, s3, v14
	v_add_u32_e32 v12, 512, v0
	v_mul_u32_u24_e32 v13, 0xaaab, v12
	v_lshrrev_b32_e32 v13, 22, v13
	v_mul_u32_u24_e32 v14, 0x60, v13
	v_sub_u32_e32 v14, v12, v14
	v_lshlrev_b32_e32 v14, 4, v14
	v_mad_u32_u24 v94, v13, s3, v14
	v_add_u32_e32 v12, 768, v0
	v_mul_u32_u24_e32 v13, 0xaaab, v12
	v_lshrrev_b32_e32 v13, 22, v13
	v_mul_u32_u24_e32 v14, 0x60, v13
	v_sub_u32_e32 v14, v12, v14
	v_lshlrev_b32_e32 v14, 4, v14
	v_mad_u32_u24 v95, v13, s3, v14
	v_add_u32_e32 v12, 1024, v0
	v_mul_u32_u24_e32 v13, 0xaaab, v12
	v_lshrrev_b32_e32 v13, 22, v13
	v_mul_u32_u24_e32 v14, 0x60, v13
	v_sub_u32_e32 v14, v12, v14
	v_lshlrev_b32_e32 v14, 4, v14
	v_mad_u32_u24 v96, v13, s3, v14
	v_add_u32_e32 v12, 1280, v0
	v_mul_u32_u24_e32 v13, 0xaaab, v12
	v_lshrrev_b32_e32 v13, 22, v13
	v_mul_u32_u24_e32 v14, 0x60, v13
	v_sub_u32_e32 v14, v12, v14
	v_lshlrev_b32_e32 v14, 4, v14
	v_mad_u32_u24 v97, v13, s3, v14
	v_mov_b32_e32 v4, 0x6040
	v_lshl_add_u32 v4, v0, 2, v4
	s_waitcnt vmcnt(6)
	ds_write2_b32 v92, v68, v69 offset1:1
	ds_write2_b32 v92, v70, v71 offset0:2 offset1:3
	s_waitcnt vmcnt(5)
	ds_write2_b32 v93, v72, v73 offset1:1
	ds_write2_b32 v93, v74, v75 offset0:2 offset1:3
	s_waitcnt vmcnt(4)
	ds_write2_b32 v94, v76, v77 offset1:1
	ds_write2_b32 v94, v78, v79 offset0:2 offset1:3
	s_waitcnt vmcnt(3)
	ds_write2_b32 v95, v80, v81 offset1:1
	ds_write2_b32 v95, v82, v83 offset0:2 offset1:3
	s_waitcnt vmcnt(2)
	ds_write2_b32 v96, v84, v85 offset1:1
	ds_write2_b32 v96, v86, v87 offset0:2 offset1:3
	s_waitcnt vmcnt(1)
	ds_write2_b32 v97, v88, v89 offset1:1
	ds_write2_b32 v97, v90, v91 offset0:2 offset1:3
	s_waitcnt vmcnt(0)
	ds_write_b32 v4, v98
	s_and_saveexec_b64 s[6:7], vcc
	s_waitcnt vmcnt(0)
	ds_write_b32 v4, v99 offset:1024
	s_or_b64 exec, exec, s[6:7]
	s_movk_i32 s0, 0x180
	v_cmp_gt_u32_e64 s[0:1], s0, v0
	s_mov_b64 s[4:5], exec

	.amdhsa_kernel _Z6k_prep5PrepP
		.amdhsa_group_segment_fixed_size 27780
		.amdhsa_private_segment_fixed_size 0
		.amdhsa_kernarg_size 272
		.amdhsa_user_sgpr_count 2
		.amdhsa_user_sgpr_dispatch_ptr 0
		.amdhsa_user_sgpr_queue_ptr 0
		.amdhsa_user_sgpr_kernarg_segment_ptr 1
		.amdhsa_user_sgpr_dispatch_id 0
		.amdhsa_user_sgpr_kernarg_preload_length 0
		.amdhsa_user_sgpr_kernarg_preload_offset 0
		.amdhsa_user_sgpr_private_segment_size 0
		.amdhsa_uses_dynamic_stack 0
		.amdhsa_enable_private_segment 0
		.amdhsa_system_sgpr_workgroup_id_x 1
		.amdhsa_system_sgpr_workgroup_id_y 1
		.amdhsa_system_sgpr_workgroup_id_z 0
		.amdhsa_system_sgpr_workgroup_info 0
		.amdhsa_system_vgpr_workitem_id 0
		.amdhsa_next_free_vgpr 135
		.amdhsa_next_free_sgpr 100
		.amdhsa_accum_offset 136
		.amdhsa_reserve_vcc 1
		.amdhsa_float_round_mode_32 0
		.amdhsa_float_round_mode_16_64 0
		.amdhsa_float_denorm_mode_32 3
		.amdhsa_float_denorm_mode_16_64 3
		.amdhsa_dx10_clamp 1
		.amdhsa_ieee_mode 1
		.amdhsa_fp16_overflow 0
		.amdhsa_tg_split 0
		.amdhsa_exception_fp_ieee_invalid_op 0
		.amdhsa_exception_fp_denorm_src 0
		.amdhsa_exception_fp_ieee_div_zero 0
		.amdhsa_exception_fp_ieee_overflow 0
		.amdhsa_exception_fp_ieee_underflow 0
		.amdhsa_exception_fp_ieee_inexact 0
		.amdhsa_exception_int_div_zero 0
	.end_amdhsa_kernel

amdhsa.kernels:
  - .agpr_count:     0
    .args:
      - .offset:         0
        .size:           272
        .value_kind:     by_value
    .group_segment_fixed_size: 27780
    .kernarg_segment_align: 8
    .kernarg_segment_size: 272
    .language:       OpenCL C
    .language_version:
      - 2
      - 0
    .max_flat_workgroup_size: 1024
    .name:           _Z6k_prep5PrepP
    .private_segment_fixed_size: 0
    .sgpr_count:     106
    .sgpr_spill_count: 0
    .symbol:         _Z6k_prep5PrepP.kd
    .uniform_work_group_size: 1
    .uses_dynamic_stack: false
    .vgpr_count:     135
    .vgpr_spill_count: 0
    .wavefront_size: 64
  - .agpr_count:     0
    .args:
      - .actual_access:  read_only
        .address_space:  global
        .offset:         0
        .size:           8
        .value_kind:     global_buffer
      - .actual_access:  read_only
        .address_space:  global
        .offset:         8
        .size:           8
        .value_kind:     global_buffer
      - .actual_access:  read_only
        .address_space:  global
        .offset:         16
        .size:           8
        .value_kind:     global_buffer
      - .address_space:  global
        .offset:         24
        .size:           8
        .value_kind:     global_buffer
      - .actual_access:  read_only
        .address_space:  global
        .offset:         32
        .size:           8
        .value_kind:     global_buffer
      - .actual_access:  read_only
        .address_space:  global
        .offset:         40
        .size:           8
        .value_kind:     global_buffer
      - .actual_access:  read_only
        .address_space:  global
        .offset:         48
        .size:           8
        .value_kind:     global_buffer
      - .actual_access:  read_only
        .address_space:  global
        .offset:         56
        .size:           8
        .value_kind:     global_buffer
      - .actual_access:  write_only
        .address_space:  global
        .offset:         64
        .size:           8
        .value_kind:     global_buffer
    .group_segment_fixed_size: 0
    .kernarg_segment_align: 8
    .kernarg_segment_size: 72
    .language:       OpenCL C
    .language_version:
      - 2
      - 0
    .max_flat_workgroup_size: 384
    .name:           _Z11k1_temporalPKfS0_S0_PKDF16_S0_S0_S0_S0_Pf
    .private_segment_fixed_size: 0
    .sgpr_count:     34
    .sgpr_spill_count: 0
    .symbol:         _Z11k1_temporalPKfS0_S0_PKDF16_S0_S0_S0_S0_Pf.kd
    .uniform_work_group_size: 1
    .uses_dynamic_stack: false
    .vgpr_count:     247
    .vgpr_spill_count: 0
    .wavefront_size: 64
  - .agpr_count:     0
    .args:
      - .address_space:  global
        .offset:         0
        .size:           8
        .value_kind:     global_buffer
      - .address_space:  global
        .offset:         8
        .size:           8
        .value_kind:     global_buffer
      - .actual_access:  read_only
        .address_space:  global
        .offset:         16
        .size:           8
        .value_kind:     global_buffer
      - .actual_access:  read_only
        .address_space:  global
        .offset:         24
        .size:           8
        .value_kind:     global_buffer
      - .actual_access:  read_only
        .address_space:  global
        .offset:         32
        .size:           8
        .value_kind:     global_buffer
      - .actual_access:  read_only
        .address_space:  global
        .offset:         40
        .size:           8
        .value_kind:     global_buffer
      - .actual_access:  read_only
        .address_space:  global
        .offset:         48
        .size:           8
        .value_kind:     global_buffer
      - .actual_access:  read_only
        .address_space:  global
        .offset:         56
        .size:           8
        .value_kind:     global_buffer
      - .actual_access:  read_only
        .address_space:  global
        .offset:         64
        .size:           8
        .value_kind:     global_buffer
      - .actual_access:  read_only
        .address_space:  global
        .offset:         72
        .size:           8
        .value_kind:     global_buffer
      - .actual_access:  read_only
        .address_space:  global
        .offset:         80
        .size:           8
        .value_kind:     global_buffer
      - .actual_access:  read_only
        .address_space:  global
        .offset:         88
        .size:           8
        .value_kind:     global_buffer
      - .actual_access:  read_only
        .address_space:  global
        .offset:         96
        .size:           8
        .value_kind:     global_buffer
      - .actual_access:  read_only
        .address_space:  global
        .offset:         104
        .size:           8
        .value_kind:     global_buffer
      - .actual_access:  read_only
        .address_space:  global
        .offset:         112
        .size:           8
        .value_kind:     global_buffer
      - .actual_access:  read_only
        .address_space:  global
        .offset:         120
        .size:           8
        .value_kind:     global_buffer
      - .address_space:  global
        .offset:         128
        .size:           8
        .value_kind:     global_buffer
      - .actual_access:  write_only
        .address_space:  global
        .offset:         136
        .size:           8
        .value_kind:     global_buffer
      - .actual_access:  write_only
        .address_space:  global
        .offset:         144
        .size:           8
        .value_kind:     global_buffer
      - .actual_access:  write_only
        .address_space:  global
        .offset:         152
        .size:           8
        .value_kind:     global_buffer
      - .actual_access:  write_only
        .address_space:  global
        .offset:         160
        .size:           8
        .value_kind:     global_buffer
    .group_segment_fixed_size: 0
    .kernarg_segment_align: 8
    .kernarg_segment_size: 168
    .language:       OpenCL C
    .language_version:
      - 2
      - 0
    .max_flat_workgroup_size: 512
    .name:           _Z10k2_featurePKfPKDF16_S0_S0_S0_S0_S0_S0_PKyS0_S0_S0_S0_S0_S0_S0_PfS5_S5_S5_S5_
    .private_segment_fixed_size: 0
    .sgpr_count:     38
    .sgpr_spill_count: 0
    .symbol:         _Z10k2_featurePKfPKDF16_S0_S0_S0_S0_S0_S0_PKyS0_S0_S0_S0_S0_S0_S0_PfS5_S5_S5_S5_.kd
    .uniform_work_group_size: 1
    .uses_dynamic_stack: false
    .vgpr_count:     256
    .vgpr_spill_count: 0
    .wavefront_size: 64
  - .agpr_count:     0
    .args:
      - .actual_access:  read_only
        .address_space:  global
        .offset:         0
        .size:           8
        .value_kind:     global_buffer
      - .actual_access:  read_only
        .address_space:  global
        .offset:         8
        .size:           8
        .value_kind:     global_buffer
      - .actual_access:  read_only
        .address_space:  global
        .offset:         16
        .size:           8
        .value_kind:     global_buffer
      - .actual_access:  read_only
        .address_space:  global
        .offset:         24
        .size:           8
        .value_kind:     global_buffer
      - .actual_access:  read_only
        .address_space:  global
        .offset:         32
        .size:           8
        .value_kind:     global_buffer
      - .actual_access:  write_only
        .address_space:  global
        .offset:         40
        .size:           8
        .value_kind:     global_buffer
      - .actual_access:  write_only
        .address_space:  global
        .offset:         48
        .size:           8
        .value_kind:     global_buffer
      - .address_space:  global
        .offset:         56
        .size:           8
        .value_kind:     global_buffer
      - .actual_access:  write_only
        .address_space:  global
        .offset:         64
        .size:           8
        .value_kind:     global_buffer
    .group_segment_fixed_size: 56768
    .kernarg_segment_align: 8
    .kernarg_segment_size: 72
    .language:       OpenCL C
    .language_version:
      - 2
      - 0
    .max_flat_workgroup_size: 768
    .name:           _Z5k3_vqPKDF16_S0_S0_S0_PKfPiPfS3_S4_
    .private_segment_fixed_size: 0
    .sgpr_count:     54
    .sgpr_spill_count: 0
    .symbol:         _Z5k3_vqPKDF16_S0_S0_S0_PKfPiPfS3_S4_.kd
    .uniform_work_group_size: 1
    .uses_dynamic_stack: false
    .vgpr_count:     72
    .vgpr_spill_count: 0
    .wavefront_size: 64
  - .agpr_count:     0
    .args:
      - .actual_access:  read_only
        .address_space:  global
        .offset:         0
        .size:           8
        .value_kind:     global_buffer
      - .actual_access:  read_only
        .address_space:  global
        .offset:         8
        .size:           8
        .value_kind:     global_buffer
      - .address_space:  global
        .offset:         16
        .size:           8
        .value_kind:     global_buffer
      - .actual_access:  read_only
        .address_space:  global
        .offset:         24
        .size:           8
        .value_kind:     global_buffer
      - .actual_access:  read_only
        .address_space:  global
        .offset:         32
        .size:           8
        .value_kind:     global_buffer
      - .actual_access:  read_only
        .address_space:  global
        .offset:         40
        .size:           8
        .value_kind:     global_buffer
      - .actual_access:  read_only
        .address_space:  global
        .offset:         48
        .size:           8
        .value_kind:     global_buffer
      - .actual_access:  read_only
        .address_space:  global
        .offset:         56
        .size:           8
        .value_kind:     global_buffer
      - .actual_access:  read_only
        .address_space:  global
        .offset:         64
        .size:           8
        .value_kind:     global_buffer
      - .actual_access:  read_only
        .address_space:  global
        .offset:         72
        .size:           8
        .value_kind:     global_buffer
      - .actual_access:  read_only
        .address_space:  global
        .offset:         80
        .size:           8
        .value_kind:     global_buffer
      - .address_space:  global
        .offset:         88
        .size:           8
        .value_kind:     global_buffer
      - .actual_access:  read_only
        .address_space:  global
        .offset:         96
        .size:           8
        .value_kind:     global_buffer
      - .actual_access:  read_only
        .address_space:  global
        .offset:         104
        .size:           8
        .value_kind:     global_buffer
      - .actual_access:  read_only
        .address_space:  global
        .offset:         112
        .size:           8
        .value_kind:     global_buffer
      - .actual_access:  read_only
        .address_space:  global
        .offset:         120
        .size:           8
        .value_kind:     global_buffer
      - .actual_access:  read_only
        .address_space:  global
        .offset:         128
        .size:           8
        .value_kind:     global_buffer
      - .address_space:  global
        .offset:         136
        .size:           8
        .value_kind:     global_buffer
      - .address_space:  global
        .offset:         144
        .size:           8
        .value_kind:     global_buffer
      - .actual_access:  write_only
        .address_space:  global
        .offset:         152
        .size:           8
        .value_kind:     global_buffer
      - .offset:         160
        .size:           4
        .value_kind:     hidden_block_count_x
      - .offset:         164
        .size:           4
        .value_kind:     hidden_block_count_y
      - .offset:         168
        .size:           4
        .value_kind:     hidden_block_count_z
      - .offset:         172
        .size:           2
        .value_kind:     hidden_group_size_x
      - .offset:         174
        .size:           2
        .value_kind:     hidden_group_size_y
      - .offset:         176
        .size:           2
        .value_kind:     hidden_group_size_z
      - .offset:         178
        .size:           2
        .value_kind:     hidden_remainder_x
      - .offset:         180
        .size:           2
        .value_kind:     hidden_remainder_y
      - .offset:         182
        .size:           2
        .value_kind:     hidden_remainder_z
      - .offset:         200
        .size:           8
        .value_kind:     hidden_global_offset_x
      - .offset:         208
        .size:           8
        .value_kind:     hidden_global_offset_y
      - .offset:         216
        .size:           8
        .value_kind:     hidden_global_offset_z
      - .offset:         224
        .size:           2
        .value_kind:     hidden_grid_dims
      - .offset:         280
        .size:           4
        .value_kind:     hidden_dynamic_lds_size
    .group_segment_fixed_size: 0
    .kernarg_segment_align: 8
    .kernarg_segment_size: 416
    .language:       OpenCL C
    .language_version:
      - 2
      - 0
    .max_flat_workgroup_size: 768
    .name:           _Z7k5_convPKDF16_PKiS0_PKfS4_S4_S4_S4_S4_S4_S4_PfS4_S4_S2_S2_S4_PiS5_S5_
    .private_segment_fixed_size: 0
    .sgpr_count:     51
    .sgpr_spill_count: 0
    .symbol:         _Z7k5_convPKDF16_PKiS0_PKfS4_S4_S4_S4_S4_S4_S4_PfS4_S4_S2_S2_S4_PiS5_S5_.kd
    .uniform_work_group_size: 1
    .uses_dynamic_stack: false
    .vgpr_count:     80
    .vgpr_spill_count: 0
    .wavefront_size: 64
